# s9
# speedup vs baseline: 1.0368x; 1.0107x over previous
.LBB1_1:
	s_or_b64 exec, exec, s[0:1]
	s_add_u32 s2, s2, 0x800000
	s_addc_u32 s3, s3, 0
	s_addk_i32 s76, 0x800
	s_add_i32 s77, s77, 8
	s_addk_i32 s78, 0x400
	s_add_i32 s89, s89, 8
	s_cmp_eq_u32 s2, 0x2000000
	s_waitcnt vmcnt(0) lgkmcnt(0)
	s_cbranch_scc1 .LBB1_27

.LBB1_7:
	s_or_b64 exec, exec, s[0:1]
	ds_read_b128 v[134:137], v131 offset:32768
	ds_read_b128 v[138:141], v131 offset:34816
	ds_read_b128 v[142:145], v131 offset:36864
	ds_read_b128 v[148:151], v131 offset:38912
	ds_read_b128 v[152:155], v129 offset:32768
	ds_read_b128 v[156:159], v129 offset:34816
	s_setprio 1
	s_waitcnt lgkmcnt(0)
	v_mfma_f32_16x16x32_f16 v[0:3], v[152:155], v[134:137], v[0:3]
	v_mfma_f32_16x16x32_f16 v[4:7], v[152:155], v[138:141], v[4:7]
	v_mfma_f32_16x16x32_f16 v[8:11], v[152:155], v[142:145], v[8:11]
	v_mfma_f32_16x16x32_f16 v[12:15], v[152:155], v[148:151], v[12:15]
	v_mfma_f32_16x16x32_f16 v[16:19], v[156:159], v[134:137], v[16:19]
	v_mfma_f32_16x16x32_f16 v[20:23], v[156:159], v[138:141], v[20:23]
	v_mfma_f32_16x16x32_f16 v[36:39], v[156:159], v[142:145], v[36:39]
	v_mfma_f32_16x16x32_f16 v[40:43], v[156:159], v[148:151], v[40:43]
	s_setprio 0
	ds_read_b128 v[152:155], v129 offset:36864
	ds_read_b128 v[156:159], v129 offset:38912
	s_setprio 1
	s_waitcnt lgkmcnt(0)
	v_mfma_f32_16x16x32_f16 v[24:27], v[152:155], v[134:137], v[24:27]
	v_mfma_f32_16x16x32_f16 v[44:47], v[152:155], v[138:141], v[44:47]
	v_mfma_f32_16x16x32_f16 v[172:175], v[156:159], v[142:145], v[64:67]
	v_mfma_f32_16x16x32_f16 v[66:69], v[156:159], v[148:151], v[68:71]
	v_mfma_f32_16x16x32_f16 v[160:163], v[152:155], v[142:145], v[48:51]
	v_mfma_f32_16x16x32_f16 v[152:155], v[152:155], v[148:151], v[52:55]
	v_mfma_f32_16x16x32_f16 v[164:167], v[156:159], v[134:137], v[56:59]
	v_mfma_f32_16x16x32_f16 v[168:171], v[156:159], v[138:141], v[60:63]
	s_setprio 0
	ds_read_b128 v[48:51], v129 offset:40960
	ds_read_b128 v[52:55], v129 offset:43008
	s_setprio 1
	s_waitcnt lgkmcnt(0)
	v_mfma_f32_16x16x32_f16 v[28:31], v[48:51], v[134:137], v[28:31]
	v_mfma_f32_16x16x32_f16 v[70:73], v[48:51], v[138:141], v[72:75]
	v_mfma_f32_16x16x32_f16 v[74:77], v[48:51], v[142:145], v[76:79]
	v_mfma_f32_16x16x32_f16 v[78:81], v[48:51], v[148:151], v[80:83]
	v_mfma_f32_16x16x32_f16 v[82:85], v[52:55], v[134:137], v[84:87]
	v_mfma_f32_16x16x32_f16 v[86:89], v[52:55], v[138:141], v[88:91]
	v_mfma_f32_16x16x32_f16 v[90:93], v[52:55], v[142:145], v[92:95]
	v_mfma_f32_16x16x32_f16 v[94:97], v[52:55], v[148:151], v[96:99]
	s_setprio 0
	ds_read_b128 v[48:51], v129 offset:45056
	ds_read_b128 v[52:55], v129 offset:47104
	s_setprio 1
	s_waitcnt lgkmcnt(0)
	v_mfma_f32_16x16x32_f16 v[202:205], v[52:55], v[138:141], v[116:119]
	v_mfma_f32_16x16x32_f16 v[206:209], v[52:55], v[142:145], v[120:123]
	v_mfma_f32_16x16x32_f16 v[156:159], v[48:51], v[134:137], v[32:35]
	v_mfma_f32_16x16x32_f16 v[176:179], v[48:51], v[138:141], v[100:103]
	v_mfma_f32_16x16x32_f16 v[180:183], v[48:51], v[142:145], v[104:107]
	v_mfma_f32_16x16x32_f16 v[184:187], v[48:51], v[148:151], v[108:111]
	v_mfma_f32_16x16x32_f16 v[188:191], v[52:55], v[134:137], v[112:115]
	v_mfma_f32_16x16x32_f16 v[148:151], v[52:55], v[148:151], v[124:127]
	s_setprio 0
	ds_read_b128 v[210:213], v128 offset:32768
	ds_read_b128 v[214:217], v128 offset:34816
	ds_read_b128 v[218:221], v128 offset:36864
	ds_read_b128 v[222:225], v128 offset:38912
	ds_read_b128 v[32:35], v130 offset:32768
	ds_read_b128 v[98:101], v130 offset:34816
	s_setprio 1
	s_waitcnt lgkmcnt(0)
	v_mfma_f32_16x16x32_f16 v[50:53], v[32:35], v[210:213], v[0:3]
	v_mfma_f32_16x16x32_f16 v[54:57], v[32:35], v[214:217], v[4:7]
	v_mfma_f32_16x16x32_f16 v[58:61], v[32:35], v[218:221], v[8:11]
	v_mfma_f32_16x16x32_f16 v[62:65], v[32:35], v[222:225], v[12:15]
	v_mfma_f32_16x16x32_f16 v[142:145], v[98:101], v[210:213], v[16:19]
	v_mfma_f32_16x16x32_f16 v[138:141], v[98:101], v[214:217], v[20:23]
	v_mfma_f32_16x16x32_f16 v[134:137], v[98:101], v[218:221], v[36:39]
	v_mfma_f32_16x16x32_f16 v[126:129], v[98:101], v[222:225], v[40:43]
	s_setprio 0
	ds_read_b128 v[0:3], v130 offset:36864
	ds_read_b128 v[4:7], v130 offset:38912
	s_setprio 1
	s_waitcnt lgkmcnt(0)
	v_mfma_f32_16x16x32_f16 v[34:37], v[0:3], v[210:213], v[24:27]
	v_mfma_f32_16x16x32_f16 v[38:41], v[0:3], v[214:217], v[44:47]
	v_mfma_f32_16x16x32_f16 v[42:45], v[0:3], v[218:221], v[160:163]
	v_mfma_f32_16x16x32_f16 v[46:49], v[0:3], v[222:225], v[152:155]
	v_mfma_f32_16x16x32_f16 v[122:125], v[4:7], v[210:213], v[164:167]
	v_mfma_f32_16x16x32_f16 v[118:121], v[4:7], v[214:217], v[168:171]
	v_mfma_f32_16x16x32_f16 v[114:117], v[4:7], v[218:221], v[172:175]
	v_mfma_f32_16x16x32_f16 v[110:113], v[4:7], v[222:225], v[66:69]
	s_setprio 0
	ds_read_b128 v[10:13], v130 offset:40960
	ds_read_b128 v[18:21], v130 offset:43008
	s_setprio 1
	s_waitcnt lgkmcnt(0)
	v_mfma_f32_16x16x32_f16 v[2:5], v[10:13], v[210:213], v[28:31]
	v_mfma_f32_16x16x32_f16 v[6:9], v[10:13], v[214:217], v[70:73]
	v_mfma_f32_16x16x32_f16 v[14:17], v[10:13], v[218:221], v[74:77]
	v_mfma_f32_16x16x32_f16 v[30:33], v[10:13], v[222:225], v[78:81]
	v_mfma_f32_16x16x32_f16 v[106:109], v[18:21], v[210:213], v[82:85]
	v_mfma_f32_16x16x32_f16 v[102:105], v[18:21], v[214:217], v[86:89]
	v_mfma_f32_16x16x32_f16 v[98:101], v[18:21], v[218:221], v[90:93]
	v_mfma_f32_16x16x32_f16 v[86:89], v[18:21], v[222:225], v[94:97]
	s_setprio 0
	ds_read_b128 v[26:29], v130 offset:45056
	ds_read_b128 v[66:69], v130 offset:47104
	s_setprio 1
	s_waitcnt lgkmcnt(0)
	v_mfma_f32_16x16x32_f16 v[10:13], v[26:29], v[210:213], v[156:159]
	v_mfma_f32_16x16x32_f16 v[18:21], v[26:29], v[214:217], v[176:179]
	v_mfma_f32_16x16x32_f16 v[22:25], v[26:29], v[218:221], v[180:183]
	v_mfma_f32_16x16x32_f16 v[26:29], v[26:29], v[222:225], v[184:187]
	v_mfma_f32_16x16x32_f16 v[78:81], v[66:69], v[210:213], v[188:191]
	v_mfma_f32_16x16x32_f16 v[74:77], v[66:69], v[214:217], v[202:205]
	v_mfma_f32_16x16x32_f16 v[70:73], v[66:69], v[218:221], v[206:209]
	v_mfma_f32_16x16x32_f16 v[66:69], v[66:69], v[222:225], v[148:151]
	s_setprio 0
	s_waitcnt vmcnt(0)
	s_waitcnt lgkmcnt(0)
	s_waitcnt vmcnt(0)
	s_barrier
	v_lshrrev_b32 v0, 4, v194
	s_nop 0
	v_and_b32_e32 v204, 63, v0
	v_lshlrev_b32_e32 v82, 2, v204
	v_ashrrev_i32_e32 v1, 6, v0
	v_cmp_gt_i32_e32 vcc, s82, v0
	v_xor_b32_e32 v205, 0x80, v82
	v_xor_b32_e32 v206, 64, v82
	s_and_saveexec_b64 s[0:1], vcc
	s_cbranch_execz .LBB1_10
	v_sub_f32_e64 v83, v146, |v146|
	v_cmp_eq_u32_e32 vcc, 63, v204
	v_lshlrev_b32_e32 v85, 2, v0
	v_mul_f32_e32 v84, -2.0, v146
	s_nop 1
	v_add_f32_dpp v83, v83, v83 quad_perm:[1,0,3,2] row_mask:0xf bank_mask:0xf
	s_nop 1
	v_add_f32_dpp v83, v83, v83 quad_perm:[2,3,0,1] row_mask:0xf bank_mask:0xf
	s_nop 1
	v_add_f32_dpp v83, v83, v83 row_half_mirror row_mask:0xf bank_mask:0xf
	s_nop 1
	v_add_f32_dpp v83, v83, v83 row_mirror row_mask:0xf bank_mask:0xf
	s_nop 1
	v_add_f32_dpp v83, v83, v83 row_bcast:15 row_mask:0xa bank_mask:0xf
	s_nop 1
	v_add_f32_dpp v83, v83, v83 row_bcast:31 row_mask:0xc bank_mask:0xf
	ds_write2st64_b32 v85, v133, v84 offset0:128 offset1:132
	ds_write_b32 v85, v132 offset:34816
	v_mov_b32_e32 v82, v83
	v_lshlrev_b32_e32 v83, 2, v1
	s_and_b64 exec, exec, vcc
	s_cbranch_execz .LBB1_10
	ds_write_b32 v83, v82 offset:35840
